# attention Q-fragment and partial-O loads carry the nt streaming hint (read once per phase)
# baseline (speedup 1.0000x reference)
; #define LAS __attribute__((address_space(3)))
; #define AT_SU(s_) (2 * AT_P((s_) >> 1) + ((s_) & 1))
; #define AT_OK(s_) ((s_) < ns && AT_P((s_) >> 1) < NP)
; #define AT_FETCH_Q(su_) do { const int su__ = (su_); const bf16* qp_ = QK + ((((size_t)((su__ >> 8) * 16 + ((su__ >> 4) & 15)) << ldil) | ((su__ >> lq4) & dilm)) * Ls + ((su__ & nq4m) * 128 + 16 * wq + n)) * 64 + 8 * kq; \
;         qf[0] = *(const bf16x8s*)qp_; qf[1] = *(const bf16x8s*)(qp_ + 32); } while (0)
; #define AT_SU(s_) (2 * AT_P((s_) >> 1) + ((s_) & 1))
; #define AT_FETCH_Q(su_) do { const int su__ = (su_); const bf16* qp_ = QK + ((((size_t)((su__ >> 8) * 16 + ((su__ >> 4) & 15)) << ldil) | ((su__ >> lq4) & dilm)) * Ls + ((su__ & nq4m) * 128 + 16 * wq + n)) * 64 + 8 * kq; \
;         qf[0] = *(const bf16x8s*)qp_; qf[1] = *(const bf16x8s*)(qp_ + 32); tick += 2; } while (0)
; __device__ __forceinline__ void attn_group_mfma5(const bf16* QK, const float* bias2g, int ldil, int first, bf16* OACC, float* LSE, LAS unsigned char* lds, const int tid, const int bid, const int G) {
;     ...
;     bf16x8s qf[2]; float bv = 0.f;
;     if (AT_OK(0)) { bv = AT_BIAS(AT_SU(0)); AT_DMA(AT_SU(0), 0); AT_FETCH_Q(AT_SU(0)); if (tid < 192) ((LAS float*)(lds + 65536))[tid] = bv; }
.LBB0_179:
	s_ashr_i32 s4, s6, 3
	s_and_b32 s4, s4, -16
	s_bfe_u32 s5, s6, 0x40003
	s_lshl_b32 s7, s6, 1
	s_or_b32 s4, s4, s5
	s_ashr_i32 s5, s4, 31
	s_ashr_i32 s6, s7, s39
	s_lshl_b64 s[4:5], s[4:5], s43
	s_and_b32 s6, s6, s49
	s_or_b32 s4, s4, s6
	s_lshl_b64 s[4:5], s[4:5], s0
	s_and_b32 s0, s7, s48
	s_lshl_b32 s0, s0, 7
	s_lshl_b32 s6, s1, 4
	s_add_i32 s0, s0, s6
	v_or_b32_e32 v0, s0, v67
	v_ashrrev_i32_e32 v1, 31, v0
	v_lshl_add_u64 v[0:1], s[4:5], 0, v[0:1]
	v_lshlrev_b64 v[0:1], 7, v[0:1]
	v_lshl_add_u64 v[0:1], s[80:81], 0, v[0:1]
	v_lshlrev_b32_e32 v2, 4, v51
	v_lshl_add_u64 v[0:1], v[0:1], 0, v[2:3]
	global_load_dwordx4 v[4:7], v[0:1], off nt
	global_load_dwordx4 v[8:11], v[0:1], off offset:64 nt
	s_movk_i32 s0, 0xc0
	v_cmp_gt_i32_e32 vcc, s0, v68
	s_and_saveexec_b64 s[4:5], vcc
	s_cbranch_execz .LBB0_181
	v_lshl_add_u32 v0, v68, 2, 0
	v_add_u32_e32 v0, 0x10000, v0
	s_waitcnt vmcnt(0)
	ds_write_b32 v0, v70

; #define AT_SU(s_) (2 * AT_P((s_) >> 1) + ((s_) & 1))
; #define AT_FETCH_Q(su_) do { const int su__ = (su_); const bf16* qp_ = QK + ((((size_t)((su__ >> 8) * 16 + ((su__ >> 4) & 15)) << ldil) | ((su__ >> lq4) & dilm)) * Ls + ((su__ & nq4m) * 128 + 16 * wq + n)) * 64 + 8 * kq; \
;         qf[0] = *(const bf16x8s*)qp_; qf[1] = *(const bf16x8s*)(qp_ + 32); } while (0)
; #define AT_SU(s_) (2 * AT_P((s_) >> 1) + ((s_) & 1))
; #define AT_FETCH_Q(su_) do { const int su__ = (su_); const bf16* qp_ = QK + ((((size_t)((su__ >> 8) * 16 + ((su__ >> 4) & 15)) << ldil) | ((su__ >> lq4) & dilm)) * Ls + ((su__ & nq4m) * 128 + 16 * wq + n)) * 64 + 8 * kq; \
;         qf[0] = *(const bf16x8s*)qp_; qf[1] = *(const bf16x8s*)(qp_ + 32); tick += 2; } while (0)
; __device__ __forceinline__ void attn_group_mfma5(const bf16* QK, const float* bias2g, int ldil, int first, bf16* OACC, float* LSE, LAS unsigned char* lds, const int tid, const int bid, const int G) {
;     ...
;         if (more) AT_FETCH_Q(AT_SU(s + 1));
;         float lold = 0.f; v2u xo[4];
;         if (!first) { lold = LSE[rowq * 16 + h];
; #pragma unroll
;             for (int db = 0; db < 4; ++db) xo[db] = *(const v2u*)(OACC + rowq * D + h * 64 + 16 * db + 4 * kq); }
.LBB0_214:
	s_lshl_b32 s0, s37, 1
	s_and_b32 s8, s77, 1
	s_or_b32 s0, s0, s8
	s_ashr_i32 s8, s37, 3
	s_and_b32 s8, s8, -16
	s_bfe_u32 s9, s37, 0x40003
	s_or_b32 s8, s8, s9
	s_ashr_i32 s9, s8, 31
	s_ashr_i32 s37, s0, s39
	s_lshl_b64 s[8:9], s[8:9], s43
	s_and_b32 s37, s37, s49
	s_and_b32 s0, s0, s48
	s_or_b32 s8, s8, s37
	v_lshl_add_u32 v0, s0, 7, v71
	s_lshl_b64 s[8:9], s[8:9], s58
	v_ashrrev_i32_e32 v1, 31, v0
	v_lshl_add_u64 v[0:1], s[8:9], 0, v[0:1]
	v_lshlrev_b64 v[0:1], 7, v[0:1]
	v_lshl_add_u64 v[0:1], v[48:49], 0, v[0:1]
	global_load_dwordx4 v[4:7], v[0:1], off nt
	global_load_dwordx4 v[8:11], v[0:1], off offset:64 nt
.LBB0_215:
	s_lshl_b32 s0, s42, 1
	s_or_b32 s0, s0, s36
	s_and_b32 s36, s0, s48
	s_ashr_i32 s8, s42, 7
	s_ashr_i32 s0, s0, s39
	s_ashr_i32 s9, s8, 31
	s_lshl_b32 s36, s36, 7
	s_and_b32 s0, s0, s49
	s_lshl_b64 s[8:9], s[8:9], 11
	v_add_u32_e32 v0, s36, v71
	v_ashrrev_i32_e32 v1, 31, v0
	s_add_u32 s8, s8, s0
	s_addc_u32 s9, s9, 0
	v_lshlrev_b64 v[0:1], s43, v[0:1]
	v_lshl_add_u64 v[0:1], s[8:9], 0, v[0:1]
	v_cndmask_b32_e64 v2, 0, 1, s[44:45]
	v_and_b32_e32 v52, 0xfffff800, v0
	v_and_b32_e32 v53, 3, v0
	v_lshlrev_b32_e32 v52, 6, v52
	v_lshl_or_b32 v52, v53, 11, v52
	v_and_b32_e32 v53, 0x7fc, v0
	v_or_b32_e32 v52, v52, v53
	v_mov_b32_e32 v53, 0
	v_lshlrev_b64 v[0:1], 11, v[0:1]
	s_bfe_u32 s0, s42, 0x40003
	v_cmp_ne_u32_e64 s[8:9], 1, v2
	s_andn2_b64 vcc, exec, s[44:45]
	v_lshl_add_u64 v[62:63], s[52:53], 0, v[52:53]
	v_lshl_add_u64 v[60:61], s[46:47], 0, v[0:1]
	v_lshlrev_b32_e32 v58, 1, v50
	s_cbranch_vccnz .LBB0_217
	s_lshl_b32 s60, s0, 13
	v_lshl_add_u64 v[0:1], v[62:63], 0, s[60:61]
	s_lshl_b32 s60, s0, 7
	v_lshl_add_u64 v[52:53], v[60:61], 0, s[60:61]
	v_mov_b32_e32 v59, v3
	v_lshl_add_u64 v[52:53], v[52:53], 0, v[58:59]
	v_lshl_add_u64 v[114:115], v[52:53], 0, v[112:113]
	global_load_dword v59, v[0:1], off
	global_load_dwordx4 v[104:107], v[114:115], off nt
	global_load_dwordx4 v[108:111], v[114:115], off offset:64 nt
	s_branch .LBB0_218

; #define LAS __attribute__((address_space(3)))
; #define AT_SU(s_) (2 * AT_P((s_) >> 1) + ((s_) & 1))
; #define AT_FETCH_Q(su_) do { const int su__ = (su_); const bf16* qp_ = QK + ((((size_t)((su__ >> 8) * 16 + ((su__ >> 4) & 15)) << ldil) | ((su__ >> lq4) & dilm)) * Ls + ((su__ & nq4m) * 128 + 16 * wq + n)) * 64 + 8 * kq; \
;         qf[0] = *(const bf16x8s*)qp_; qf[1] = *(const bf16x8s*)(qp_ + 32); } while (0)
; #define AT_SU(s_) (2 * AT_P((s_) >> 1) + ((s_) & 1))
; #define AT_FETCH_Q(su_) do { const int su__ = (su_); const bf16* qp_ = QK + ((((size_t)((su__ >> 8) * 16 + ((su__ >> 4) & 15)) << ldil) | ((su__ >> lq4) & dilm)) * Ls + ((su__ & nq4m) * 128 + 16 * wq + n)) * 64 + 8 * kq; \
;         qf[0] = *(const bf16x8s*)qp_; qf[1] = *(const bf16x8s*)(qp_ + 32); tick += 2; } while (0)
; __device__ __forceinline__ void attn_group_ring(const bf16* QK, const float* bias2g, int ldil, int first, bf16* OACC, float* LSE, LAS unsigned char* lds, const int tid, const int bid, const int G) {
;     ...
;     int tick = 0; int tkat[4] = {0, 0, 0, 0};
;     bf16x8s qf[2];
;     LAS float* const tab = (LAS float*)(lds + 131072);
;     static_assert(131072 + 768 <= RING_BYTES, "attention ring");
;     { const float bv = (tid < 192 && tid - 96 >= -64 && tid - 96 <= 64) ? bias2g[((AT_SU(0) >> 4) & 15) * 129 + tid - 96 + 64] : NEGBIG;
;       int iss0 = 0; for (; iss0 < 4 && iss0 < NH; ++iss0) AT_DMAH(iss0);
;       AT_FETCH_Q(AT_SU(0)); if (tid < 192) tab[tid] = bv; }
.LBB0_230:
	s_mov_b64 s[18:19], s[86:87]
	s_mov_b32 s17, s85
	s_or_b64 exec, exec, s[2:3]
	s_ashr_i32 s0, s0, 6
	s_sub_i32 s14, 4, s43
	s_lshl_b32 s4, -1, s14
	s_lshl_b32 s2, s0, 1
	s_ashr_i32 s1, s90, 4
	s_or_b32 s2, s2, 1
	s_andn2_b32 s8, s31, s4
	s_lshl_b32 s39, s2, 3
	s_lshl_b32 s44, s2, 10
	s_or_b32 s2, s1, 1
	s_lshl_b32 s8, s8, 7
	s_lshl_b32 s37, s0, 4
	s_lshl_b32 s3, s2, 8
	s_and_b32 s6, s31, 0xf8
	v_mov_b32_e32 v12, v66
	s_sub_i32 s8, s8, 64
	v_lshl_or_b32 v4, s2, 4, v1
	s_lshr_b32 s13, 0x800, s43
	s_lshl_b32 s5, -1, s43
	s_or_b32 s7, s3, s6
	v_ashrrev_i32_e32 v5, 31, v4
	v_ashrrev_i32_e32 v13, 3, v12
	s_add_i32 s2, s8, s37
	s_add_i32 s15, s13, -1
	s_ashr_i32 s9, s7, s14
	v_lshlrev_b64 v[4:5], s43, v[4:5]
	v_mov_b32_e32 v1, s5
	v_add_u32_e32 v2, s2, v13
	s_sub_i32 s33, 11, s43
	v_bitop3_b32 v6, v4, s9, v1 bitop3:0xf4
	v_mov_b32_e32 v7, v5
	v_min_i32_e32 v8, s15, v2
	v_cmp_lt_i32_e32 vcc, -1, v2
	v_lshlrev_b64 v[6:7], s33, v[6:7]
	s_lshl_b32 s36, s0, 11
	v_cndmask_b32_e32 v2, 0, v8, vcc
	v_lshl_add_u64 v[8:9], v[6:7], 0, v[2:3]
	v_lshrrev_b32_e32 v2, 1, v13
	v_xor_b32_e32 v2, v2, v12
	v_lshlrev_b64 v[8:9], 7, v[8:9]
	v_lshlrev_b32_e32 v2, 4, v2
	v_lshl_add_u64 v[8:9], s[80:81], 0, v[8:9]
	v_and_b32_e32 v2, 0x70, v2
	v_lshl_add_u64 v[8:9], v[8:9], 0, v[2:3]
	s_mov_b64 s[20:21], 0x8000000
	s_mov_b64 s[22:23], 0x4000000
	s_add_i32 s2, s36, 0
	v_lshl_add_u64 v[10:11], v[8:9], 0, s[20:21]
	v_lshl_add_u64 v[8:9], v[8:9], 0, s[22:23]
	s_mov_b32 m0, s2
	s_or_b32 s9, s7, 1
	global_load_lds_dwordx4 v[8:9], off nt
	v_add_u32_e32 v8, s39, v13
	v_add_u32_e32 v2, s8, v8
	v_min_i32_e32 v9, s15, v2
	v_cmp_lt_i32_e32 vcc, -1, v2
	s_add_i32 s8, s44, 0
	s_mov_b32 m0, s8
	v_cndmask_b32_e32 v2, 0, v9, vcc
	v_lshl_add_u64 v[6:7], v[6:7], 0, v[2:3]
	v_lshrrev_b32_e32 v2, 1, v8
	v_xor_b32_e32 v2, v2, v12
	v_lshlrev_b64 v[6:7], 7, v[6:7]
	v_lshlrev_b32_e32 v2, 4, v2
	v_lshl_add_u64 v[6:7], s[80:81], 0, v[6:7]
	v_and_b32_e32 v2, 0x70, v2
	v_lshl_add_u64 v[6:7], v[6:7], 0, v[2:3]
	v_lshl_add_u64 v[8:9], v[6:7], 0, s[20:21]
	v_lshl_add_u64 v[6:7], v[6:7], 0, s[22:23]
	s_andn2_b32 s10, s9, s4
	global_load_lds_dwordx4 v[6:7], off nt
	s_add_i32 m0, s2, 0x4000
	s_lshl_b32 s10, s10, 7
	global_load_lds_dwordx4 v[10:11], off nt
	s_add_i32 m0, s2, 0x4400
	s_ashr_i32 s9, s9, s14
	v_mov_b32_e32 v12, v66
	s_sub_i32 s10, s10, 64
	global_load_lds_dwordx4 v[8:9], off nt
	v_bitop3_b32 v6, v4, s9, v1 bitop3:0xf4
	v_ashrrev_i32_e32 v13, 3, v12
	s_add_i32 s9, s10, s37
	v_add_u32_e32 v2, s9, v13
	v_mov_b32_e32 v7, v5
	v_min_i32_e32 v8, s15, v2
	v_cmp_lt_i32_e32 vcc, -1, v2
	v_lshlrev_b64 v[6:7], s33, v[6:7]
	s_add_i32 m0, s2, 0x8000
	v_cndmask_b32_e32 v2, 0, v8, vcc
	v_lshl_add_u64 v[8:9], v[6:7], 0, v[2:3]
	v_lshrrev_b32_e32 v2, 1, v13
	v_xor_b32_e32 v2, v2, v12
	v_lshlrev_b64 v[8:9], 7, v[8:9]
	v_lshlrev_b32_e32 v2, 4, v2
	v_lshl_add_u64 v[8:9], s[80:81], 0, v[8:9]
	v_and_b32_e32 v2, 0x70, v2
	v_lshl_add_u64 v[8:9], v[8:9], 0, v[2:3]
	v_lshl_add_u64 v[10:11], v[8:9], 0, s[20:21]
	v_lshl_add_u64 v[8:9], v[8:9], 0, s[22:23]
	global_load_lds_dwordx4 v[8:9], off nt
	v_add_u32_e32 v8, s39, v13
	v_add_u32_e32 v2, s10, v8
	v_min_i32_e32 v9, s15, v2
	v_cmp_lt_i32_e32 vcc, -1, v2
	s_or_b32 s6, s6, 2
	s_add_i32 m0, s8, 0x8000
	v_cndmask_b32_e32 v2, 0, v9, vcc
	v_lshl_add_u64 v[6:7], v[6:7], 0, v[2:3]
	v_lshrrev_b32_e32 v2, 1, v8
	v_xor_b32_e32 v2, v2, v12
	v_lshlrev_b64 v[6:7], 7, v[6:7]
	v_lshlrev_b32_e32 v2, 4, v2
	v_lshl_add_u64 v[6:7], s[80:81], 0, v[6:7]
	v_and_b32_e32 v2, 0x70, v2
	v_lshl_add_u64 v[6:7], v[6:7], 0, v[2:3]
	v_lshl_add_u64 v[8:9], v[6:7], 0, s[20:21]
	v_lshl_add_u64 v[6:7], v[6:7], 0, s[22:23]
	s_or_b32 s3, s3, s6
	s_andn2_b32 s6, s6, s4
	global_load_lds_dwordx4 v[6:7], off nt
	s_add_i32 m0, s2, 0xc000
	s_lshl_b32 s6, s6, 7
	global_load_lds_dwordx4 v[10:11], off nt
	s_add_i32 m0, s2, 0xc400
	s_ashr_i32 s3, s3, s14
	v_mov_b32_e32 v12, v66
	s_sub_i32 s6, s6, 64
	global_load_lds_dwordx4 v[8:9], off nt
	v_bitop3_b32 v6, v4, s3, v1 bitop3:0xf4
; #define LAS __attribute__((address_space(3)))
; #define AT_SU(s_) (2 * AT_P((s_) >> 1) + ((s_) & 1))
; #define AT_FETCH_Q(su_) do { const int su__ = (su_); const bf16* qp_ = QK + ((((size_t)((su__ >> 8) * 16 + ((su__ >> 4) & 15)) << ldil) | ((su__ >> lq4) & dilm)) * Ls + ((su__ & nq4m) * 128 + 16 * wq + n)) * 64 + 8 * kq; \
;         qf[0] = *(const bf16x8s*)qp_; qf[1] = *(const bf16x8s*)(qp_ + 32); } while (0)
; #define AT_SU(s_) (2 * AT_P((s_) >> 1) + ((s_) & 1))
; #define AT_FETCH_Q(su_) do { const int su__ = (su_); const bf16* qp_ = QK + ((((size_t)((su__ >> 8) * 16 + ((su__ >> 4) & 15)) << ldil) | ((su__ >> lq4) & dilm)) * Ls + ((su__ & nq4m) * 128 + 16 * wq + n)) * 64 + 8 * kq; \
;         qf[0] = *(const bf16x8s*)qp_; qf[1] = *(const bf16x8s*)(qp_ + 32); tick += 2; } while (0)
; __device__ __forceinline__ void attn_group_ring(const bf16* QK, const float* bias2g, int ldil, int first, bf16* OACC, float* LSE, LAS unsigned char* lds, const int tid, const int bid, const int G) {
;     ...
;     int tick = 0; int tkat[4] = {0, 0, 0, 0};
;     bf16x8s qf[2];
;     LAS float* const tab = (LAS float*)(lds + 131072);
;     static_assert(131072 + 768 <= RING_BYTES, "attention ring");
;     { const float bv = (tid < 192 && tid - 96 >= -64 && tid - 96 <= 64) ? bias2g[((AT_SU(0) >> 4) & 15) * 129 + tid - 96 + 64] : NEGBIG;
;       int iss0 = 0; for (; iss0 < 4 && iss0 < NH; ++iss0) AT_DMAH(iss0);
;       AT_FETCH_Q(AT_SU(0)); if (tid < 192) tab[tid] = bv; }
	v_ashrrev_i32_e32 v13, 3, v12
	s_add_i32 s3, s6, s37
	v_add_u32_e32 v2, s3, v13
	v_mov_b32_e32 v7, v5
	v_min_i32_e32 v8, s15, v2
	v_cmp_lt_i32_e32 vcc, -1, v2
	v_lshlrev_b64 v[6:7], s33, v[6:7]
	s_add_i32 s3, 0, 0x10000
	v_cndmask_b32_e32 v2, 0, v8, vcc
	v_lshl_add_u64 v[8:9], v[6:7], 0, v[2:3]
	v_lshrrev_b32_e32 v2, 1, v13
	v_xor_b32_e32 v2, v2, v12
	v_lshlrev_b64 v[8:9], 7, v[8:9]
	v_lshlrev_b32_e32 v2, 4, v2
	v_lshl_add_u64 v[8:9], s[80:81], 0, v[8:9]
	v_and_b32_e32 v2, 0x70, v2
	v_lshl_add_u64 v[8:9], v[8:9], 0, v[2:3]
	v_lshl_add_u64 v[10:11], v[8:9], 0, s[20:21]
	v_lshl_add_u64 v[8:9], v[8:9], 0, s[22:23]
	s_add_i32 m0, s3, s36
	s_bfe_u32 s46, s90, 0x40001
	global_load_lds_dwordx4 v[8:9], off nt
	v_add_u32_e32 v8, s39, v13
	v_add_u32_e32 v2, s6, v8
	v_min_i32_e32 v9, s15, v2
	v_cmp_lt_i32_e32 vcc, -1, v2
	s_add_i32 m0, s3, s44
	s_or_b32 s3, s7, 3
	v_cndmask_b32_e32 v2, 0, v9, vcc
	v_lshl_add_u64 v[6:7], v[6:7], 0, v[2:3]
	v_lshrrev_b32_e32 v2, 1, v8
	v_xor_b32_e32 v2, v2, v12
	v_lshlrev_b64 v[6:7], 7, v[6:7]
	v_lshlrev_b32_e32 v2, 4, v2
	v_lshl_add_u64 v[6:7], s[80:81], 0, v[6:7]
	v_and_b32_e32 v2, 0x70, v2
	v_lshl_add_u64 v[6:7], v[6:7], 0, v[2:3]
	v_lshl_add_u64 v[8:9], v[6:7], 0, s[20:21]
	v_lshl_add_u64 v[6:7], v[6:7], 0, s[22:23]
	s_andn2_b32 s6, s3, s4
	global_load_lds_dwordx4 v[6:7], off nt
	s_add_i32 m0, s2, 0x14000
	s_lshl_b32 s6, s6, 7
	global_load_lds_dwordx4 v[10:11], off nt
	s_add_i32 m0, s2, 0x14400
	s_ashr_i32 s3, s3, s14
	v_mov_b32_e32 v10, v66
	s_sub_i32 s6, s6, 64
	global_load_lds_dwordx4 v[8:9], off nt
	v_bitop3_b32 v4, v4, s3, v1 bitop3:0xf4
	v_ashrrev_i32_e32 v11, 3, v10
	s_add_i32 s3, s6, s37
	v_add_u32_e32 v1, s3, v11
	v_min_i32_e32 v2, s15, v1
	v_cmp_lt_i32_e32 vcc, -1, v1
	v_lshlrev_b64 v[4:5], s33, v[4:5]
	v_lshrrev_b32_e32 v1, 1, v11
	v_cndmask_b32_e32 v2, 0, v2, vcc
	v_lshl_add_u64 v[6:7], v[4:5], 0, v[2:3]
	v_xor_b32_e32 v1, v1, v10
	v_lshlrev_b64 v[6:7], 7, v[6:7]
	v_lshlrev_b32_e32 v1, 4, v1
	v_lshl_add_u64 v[6:7], s[80:81], 0, v[6:7]
	v_and_b32_e32 v2, 0x70, v1
	v_lshl_add_u64 v[6:7], v[6:7], 0, v[2:3]
	s_add_i32 s3, 0, 0x18000
	v_add_u32_e32 v1, s39, v11
	v_lshl_add_u64 v[8:9], v[6:7], 0, s[20:21]
	v_lshl_add_u64 v[6:7], v[6:7], 0, s[22:23]
	s_add_i32 m0, s3, s36
	v_add_u32_e32 v2, s6, v1
	global_load_lds_dwordx4 v[6:7], off nt
	v_min_i32_e32 v6, s15, v2
	v_cmp_lt_i32_e32 vcc, -1, v2
	v_lshrrev_b32_e32 v1, 1, v1
	v_xor_b32_e32 v1, v1, v10
	v_cndmask_b32_e32 v2, 0, v6, vcc
	v_lshl_add_u64 v[4:5], v[4:5], 0, v[2:3]
	v_lshlrev_b64 v[4:5], 7, v[4:5]
	v_lshlrev_b32_e32 v1, 4, v1
	v_lshl_add_u64 v[4:5], s[80:81], 0, v[4:5]
	v_and_b32_e32 v2, 0x70, v1
	v_lshl_add_u64 v[4:5], v[4:5], 0, v[2:3]
	v_lshl_add_u64 v[6:7], v[4:5], 0, s[20:21]
	v_lshl_add_u64 v[4:5], v[4:5], 0, s[22:23]
	s_add_i32 m0, s3, s44
	s_and_b32 s3, s31, 0xffffff00
	global_load_lds_dwordx4 v[4:5], off nt
	s_add_i32 m0, s2, 0x1c000
	v_and_b32_e32 v2, 48, v69
	global_load_lds_dwordx4 v[8:9], off nt
	s_add_i32 m0, s2, 0x1c400
	s_lshl_b32 s2, s90, 2
	s_and_b32 s45, s2, 0x7c
	s_or_b32 s2, s3, s45
	s_bitset1_b32 s2, 7
	s_lshl_b32 s6, s2, 1
	s_ashr_i32 s2, s2, 3
	s_and_b32 s2, s2, -16
	s_or_b32 s2, s2, s46
	s_ashr_i32 s7, s6, s14
	s_andn2_b32 s6, s6, s4
	s_ashr_i32 s3, s2, 31
	s_lshl_b32 s6, s6, 7
	s_lshl_b64 s[2:3], s[2:3], s43
	s_andn2_b32 s7, s7, s5
	s_add_i32 s6, s37, s6
	s_or_b32 s2, s2, s7
	v_or_b32_e32 v4, s6, v67
	s_lshl_b64 s[2:3], s[2:3], s33
	v_ashrrev_i32_e32 v5, 31, v4
	v_lshl_add_u64 v[4:5], s[2:3], 0, v[4:5]
	v_lshlrev_b64 v[4:5], 7, v[4:5]
	v_lshl_add_u64 v[4:5], s[80:81], 0, v[4:5]
	global_load_lds_dwordx4 v[6:7], off nt
	v_lshl_add_u64 v[8:9], v[4:5], 0, v[2:3]
	global_load_dwordx4 v[4:7], v[8:9], off nt
	s_nop 0
	global_load_dwordx4 v[8:11], v[8:9], off offset:64 nt
	s_movk_i32 s2, 0xc0
	v_cmp_gt_i32_e32 vcc, s2, v68
	s_and_saveexec_b64 s[2:3], vcc
	s_cbranch_execz .LBB0_232
	v_lshl_add_u32 v1, v68, 2, 0
	v_add_u32_e32 v1, 0x20000, v1
	s_waitcnt vmcnt(0)
	ds_write_b32 v1, v0

; #define LAS __attribute__((address_space(3)))
; #define AT_SU(s_) (2 * AT_P((s_) >> 1) + ((s_) & 1))
; #define AT_FETCH_Q(su_) do { const int su__ = (su_); const bf16* qp_ = QK + ((((size_t)((su__ >> 8) * 16 + ((su__ >> 4) & 15)) << ldil) | ((su__ >> lq4) & dilm)) * Ls + ((su__ & nq4m) * 128 + 16 * wq + n)) * 64 + 8 * kq; \
;         qf[0] = *(const bf16x8s*)qp_; qf[1] = *(const bf16x8s*)(qp_ + 32); } while (0)
; #define AT_SU(s_) (2 * AT_P((s_) >> 1) + ((s_) & 1))
; #define AT_FETCH_Q(su_) do { const int su__ = (su_); const bf16* qp_ = QK + ((((size_t)((su__ >> 8) * 16 + ((su__ >> 4) & 15)) << ldil) | ((su__ >> lq4) & dilm)) * Ls + ((su__ & nq4m) * 128 + 16 * wq + n)) * 64 + 8 * kq; \
;         qf[0] = *(const bf16x8s*)qp_; qf[1] = *(const bf16x8s*)(qp_ + 32); tick += 2; } while (0)
; __device__ __forceinline__ void attn_group_ring(const bf16* QK, const float* bias2g, int ldil, int first, bf16* OACC, float* LSE, LAS unsigned char* lds, const int tid, const int bid, const int G) {
;     ...
; #pragma unroll
;         for (int ks = 0; ks < 2; ++ks)
; #pragma unroll
;             for (int kb = 0; kb < 9; ++kb) { const int wrow = 16 * (wq + kb);
;                 const LAS unsigned char* kp = lds + ((a + (wrow >> 7)) & 3) * 32768 + ((wrow & 127) + n) * 128 + (((4 * ks + kq) ^ fl) * 16);
;                 S[kb] = __builtin_amdgcn_mfma_f32_16x16x32_bf16(*(const LAS bf16x8s*)kp, qf[ks], S[kb], 0, 0, 0); }
;         __builtin_amdgcn_sched_barrier(0);
;         if (more) AT_FETCH_Q(AT_SU(s + 1));
;         float lold = 0.f; v2u xo[4];
;         if (!first) { lold = LSE[rowq * 16 + h];
; #pragma unroll
;             for (int db = 0; db < 4; ++db) xo[db] = *(const v2u*)(OACC + rowq * D + h * 64 + 16 * db + 4 * kq); }
.LBB0_238:
	s_add_i32 s42, s87, 1
	s_cmp_lt_u32 s87, 15
	s_cselect_b64 s[10:11], -1, 0
	s_add_i32 s1, s62, s87
	s_add_i32 s1, s1, s0
	s_add_i32 s71, s73, s87
	s_lshl_b32 s1, s1, 15
	s_add_i32 s71, s71, s0
	s_and_b32 s1, s1, 0x18000
	s_lshl_b32 s71, s71, 15
	v_add_u32_e32 v0, s1, v68
	s_and_b32 s1, s71, 0x18000
	v_add_u32_e32 v89, s1, v74
	s_add_i32 s1, s76, s87
	s_add_i32 s1, s1, s0
	s_add_i32 s4, s63, s87
	s_lshl_b32 s1, s1, 15
	s_add_i32 s4, s4, s0
	s_and_b32 s1, s1, 0x18000
	s_lshl_b32 s4, s4, 15
	s_add_i32 s71, s74, s87
	v_add_u32_e32 v92, s1, v77
	s_and_b32 s4, s4, 0x18000
	v_add_u32_e32 v1, v0, v69
	s_add_i32 s71, s71, s0
	v_add_u32_e32 v40, v92, v69
	ds_read_b128 v[12:15], v1
	ds_read_b128 v[40:43], v40
	v_add_u32_e32 v1, s4, v71
	s_lshl_b32 s4, s71, 15
	s_and_b32 s4, s4, 0x18000
	v_add_u32_e32 v90, s4, v75
	v_add_u32_e32 v32, v90, v69
	ds_read_b128 v[32:35], v32
	s_add_i32 s1, s77, s87
	s_add_i32 s1, s1, s0
	s_lshl_b32 s1, s1, 15
	s_and_b32 s1, s1, 0x18000
	v_add_u32_e32 v93, s1, v67
	s_waitcnt lgkmcnt(0)
	v_mfma_f32_16x16x32_bf16 v[52:55], v[32:35], v[4:7], 0
	v_add_u32_e32 v32, v93, v69
	ds_read_b128 v[32:35], v32
	v_add_u32_e32 v2, v1, v69
	v_add_u32_e32 v0, v0, v78
	ds_read_b128 v[16:19], v2
	s_waitcnt lgkmcnt(0)
	v_mfma_f32_16x16x32_bf16 v[84:87], v[32:35], v[4:7], 0
	ds_read_b128 v[32:35], v0
	s_add_i32 s5, s68, s87
	s_add_i32 s5, s5, s0
	s_lshl_b32 s5, s5, 15
	v_mfma_f32_16x16x32_bf16 v[12:15], v[12:15], v[4:7], 0
	s_and_b32 s5, s5, 0x18000
	v_add_u32_e32 v2, s5, v72
	v_add_u32_e32 v20, v2, v69
	v_add_u32_e32 v0, v1, v78
	ds_read_b128 v[20:23], v20
	s_waitcnt lgkmcnt(0)
	v_mfma_f32_16x16x32_bf16 v[44:47], v[32:35], v[8:11], v[12:15]
	s_add_i32 s70, s72, s87
	s_add_i32 s5, s75, s87
	s_add_i32 s70, s70, s0
	ds_read_b128 v[12:15], v0
	s_add_i32 s5, s5, s0
	s_lshl_b32 s70, s70, 15
	v_mfma_f32_16x16x32_bf16 v[16:19], v[16:19], v[4:7], 0
	s_lshl_b32 s5, s5, 15
	s_and_b32 s70, s70, 0x18000
	s_and_b32 s5, s5, 0x18000
	v_add_u32_e32 v88, s70, v73
	v_add_u32_e32 v91, s5, v76
	v_add_u32_e32 v24, v88, v69
	v_add_u32_e32 v36, v91, v69
	v_add_u32_e32 v0, v2, v78
	ds_read_b128 v[24:27], v24
	ds_read_b128 v[36:39], v36
	v_mfma_f32_16x16x32_bf16 v[60:63], v[40:43], v[4:7], 0
	v_add_u32_e32 v28, v89, v69
	ds_read_b128 v[28:31], v28
	s_cmp_gt_u32 s87, 14
	s_waitcnt lgkmcnt(0)
	v_mfma_f32_16x16x32_bf16 v[40:43], v[12:15], v[8:11], v[16:19]
	ds_read_b128 v[12:15], v0
	v_add_u32_e32 v0, v88, v78
	v_mfma_f32_16x16x32_bf16 v[20:23], v[20:23], v[4:7], 0
	v_mfma_f32_16x16x32_bf16 v[56:59], v[36:39], v[4:7], 0
	s_waitcnt lgkmcnt(0)
	v_mfma_f32_16x16x32_bf16 v[36:39], v[12:15], v[8:11], v[20:23]
	ds_read_b128 v[12:15], v0
	v_add_u32_e32 v0, v89, v78
	v_mfma_f32_16x16x32_bf16 v[24:27], v[24:27], v[4:7], 0
	s_waitcnt lgkmcnt(0)
	v_mfma_f32_16x16x32_bf16 v[32:35], v[12:15], v[8:11], v[24:27]
	ds_read_b128 v[12:15], v0
	v_add_u32_e32 v0, v90, v78
	v_mfma_f32_16x16x32_bf16 v[28:31], v[28:31], v[4:7], 0
	s_waitcnt lgkmcnt(0)
	v_mfma_f32_16x16x32_bf16 v[28:31], v[12:15], v[8:11], v[28:31]
	ds_read_b128 v[12:15], v0
	v_add_u32_e32 v0, v91, v78
	s_waitcnt lgkmcnt(0)
	v_mfma_f32_16x16x32_bf16 v[24:27], v[12:15], v[8:11], v[52:55]
	ds_read_b128 v[12:15], v0
	v_add_u32_e32 v0, v92, v78
	s_waitcnt lgkmcnt(0)
	v_mfma_f32_16x16x32_bf16 v[20:23], v[12:15], v[8:11], v[56:59]
	ds_read_b128 v[12:15], v0
	v_add_u32_e32 v0, v93, v78
	s_waitcnt lgkmcnt(0)
	v_mfma_f32_16x16x32_bf16 v[16:19], v[12:15], v[8:11], v[60:63]
	ds_read_b128 v[12:15], v0
	s_waitcnt lgkmcnt(0)
	v_mfma_f32_16x16x32_bf16 v[12:15], v[12:15], v[8:11], v[84:87]
	s_cbranch_scc1 .LBB0_240
	s_bfe_u32 s1, s42, 0x20001
	s_cmp_lt_u32 s87, 7
	s_cselect_b64 s[4:5], -1, 0
	v_cndmask_b32_e64 v0, 0, 1, s[4:5]
	s_add_i32 s41, s41, 2
	v_readfirstlane_b32 s4, v0
	s_or_b32 s4, s49, s4
	s_lshl_b32 s5, s4, 7
	s_or_b32 s1, s5, s1
	s_or_b32 s1, s1, s45
	s_lshl_b32 s1, s1, 1
	s_and_b32 s5, s42, 1
	s_lshl_b32 s4, s4, 4
	s_or_b32 s1, s1, s5
	s_or_b32 s4, s4, s46
	s_ashr_i32 s5, s4, 31
	s_ashr_i32 s70, s1, s14
	s_lshl_b64 s[4:5], s[4:5], s43
	s_and_b32 s70, s70, s48
	s_and_b32 s1, s1, s47
	s_or_b32 s4, s4, s70
	v_lshl_add_u32 v0, s1, 7, v64
	s_lshl_b64 s[4:5], s[4:5], s33
	v_ashrrev_i32_e32 v1, 31, v0
	v_lshl_add_u64 v[0:1], s[4:5], 0, v[0:1]
	v_lshlrev_b64 v[0:1], 7, v[0:1]
	v_lshl_add_u64 v[0:1], v[48:49], 0, v[0:1]
	global_load_dwordx4 v[4:7], v[0:1], off nt
	global_load_dwordx4 v[8:11], v[0:1], off offset:64 nt
.LBB0_240:
	s_bfe_u32 s1, s87, 0x20001
	s_cmp_lt_u32 s87, 8
	s_cselect_b64 s[4:5], -1, 0
	v_cndmask_b32_e64 v0, 0, 1, s[4:5]
	v_cndmask_b32_e64 v2, 0, 1, s[6:7]
	v_readfirstlane_b32 s4, v0
	s_or_b32 s4, s49, s4
	s_lshl_b32 s5, s4, 7
	s_or_b32 s1, s5, s1
	s_or_b32 s1, s1, s45
	s_lshl_b32 s1, s1, 1
	s_and_b32 s5, s87, 1
	s_or_b32 s1, s1, s5
	s_and_b32 s70, s1, s47
	s_ashr_i32 s1, s1, s14
	s_and_b32 s71, s1, s48
	s_lshl_b32 s1, s70, 7
	s_ashr_i32 s5, s4, 31
	v_add_u32_e32 v0, s1, v64
	s_lshl_b64 s[4:5], s[4:5], 11
	v_ashrrev_i32_e32 v1, 31, v0
	s_or_b32 s4, s4, s71
	v_lshlrev_b64 v[0:1], s43, v[0:1]
	v_lshl_add_u64 v[0:1], s[4:5], 0, v[0:1]
	v_and_b32_e32 v52, 0xfffff800, v0
	v_and_b32_e32 v53, 3, v0
	v_lshlrev_b32_e32 v52, 6, v52
	v_lshl_or_b32 v52, v53, 11, v52
	v_and_b32_e32 v53, 0x7fc, v0
	v_or_b32_e32 v52, v52, v53
	v_mov_b32_e32 v53, 0
	v_lshlrev_b64 v[0:1], 11, v[0:1]
	v_cmp_ne_u32_e64 s[4:5], 1, v2
	s_andn2_b64 vcc, exec, s[6:7]
	v_lshl_add_u64 v[60:61], s[8:9], 0, v[52:53]
	v_lshl_add_u64 v[52:53], v[50:51], 0, v[0:1]
	v_lshl_add_u64 v[114:115], v[52:53], 0, v[112:113]
	s_cbranch_vccnz .LBB0_242
	global_load_dword v84, v[60:61], off
	global_load_dwordx4 v[104:107], v[114:115], off nt
	global_load_dwordx4 v[108:111], v[114:115], off offset:64 nt
	s_branch .LBB0_243
